# union9 + GEMM K-loops: relax tests inverted at 13 phase sites so the common path falls through (was: branch to a stub + s_branch back); the rare relax path (counted wait, skip the stage) moved out of
# speedup vs baseline: 1.0126x; 1.0046x over previous
; #define PG8_STAGE(bufoff, gbase, voff) do { _Pragma("unroll") for (int _i = 0; _i < 2; ++_i) \
;         __builtin_amdgcn_global_load_lds((const unsigned*)((const char*)(gbase) + (voff)[_i]), (PG8_LAS unsigned*)(lds + (bufoff) + ldsw + _i * 8192), 16, 0, 0); } while (0)
; #define PG8_LDA(dst, b, h) do { _Pragma("unroll") for (int m = 0; m < 4; ++m) _Pragma("unroll") for (int k = 0; k < 2; ++k) dst[m][k] = *(const PG8_LAS bf16x8*)(lds + PG8_SA(b, h) + aoff + m * 2048 + k * 1024); } while (0)
; #define PG8_LDB(dst, b, h) do { _Pragma("unroll") for (int n = 0; n < 2; ++n) _Pragma("unroll") for (int k = 0; k < 2; ++k) dst[n][k] = *(const PG8_LAS bf16x8*)(lds + PG8_SB(b, h) + boff + n * 2048 + k * 1024); } while (0)
; #define PG8_MMA(ai, bj, At, Bt) do { __builtin_amdgcn_s_setprio(1); _Pragma("unroll") for (int m = 0; m < 4; ++m) _Pragma("unroll") for (int n = 0; n < 2; ++n) _Pragma("unroll") for (int k = 0; k < 2; ++k) \
;         acc[ai][bj][m][n] = mma16(Bt[n][k], At[m][k], acc[ai][bj][m][n]); __builtin_amdgcn_s_setprio(0); } while (0)
; #define PG8_WAIT_V(n) asm volatile("s_waitcnt vmcnt(" #n ")" ::: "memory")
; #define PG8_WAIT_VN(n) asm volatile("s_waitcnt vmcnt(%0)" :: "n"(n) : "memory")
; #define PG8_WAIT_L(n) asm volatile("s_waitcnt lgkmcnt(" #n ")" ::: "memory")
; #define PG8_BAR __builtin_amdgcn_s_barrier()
; #define PG8_SCHED __builtin_amdgcn_sched_barrier(0)
; template <class Epi, class Sched, bool ALIGN_EPI = false, bool SP2 = false>
; __device__ __forceinline__ void gemm_phase(PG8_LAS unsigned char* lds, const Gemm g, const Sched& S, const Epi& E, Stopwatch& sw) {
;     ...
;             int relax = __builtin_amdgcn_readfirstlane((int)((ui > 0) && (t == 0))); asm volatile("" : "+s"(relax));
;             PG8_LDB(B0, 0, 0); PG8_LDB(B1, 0, 1); PG8_SCHED; PG8_LDA(At, 0, 0); if (!relax) PG8_STAGE(PG8_SA(1, 1), a1 + hstep, voffA);
;             if (relax) PG8_WAIT_VN(8 + Epi::NST); else PG8_WAIT_V(8); PG8_WAIT_L(0); PG8_BAR; PG8_MMA(0, 0, At, B0); PG8_MMA(0, 1, At, B1); PG8_BAR; PG8_SCHED;
.LBB0_154:
	s_cmp_eq_u32 s60, 0
	s_cselect_b64 s[38:39], -1, 0
	s_and_b64 s[74:75], s[58:59], s[38:39]
	ds_read_b128 v[148:151], v228
	ds_read_b128 v[152:155], v228 offset:1024
	ds_read_b128 v[156:159], v228 offset:2048
	ds_read_b128 v[160:163], v228 offset:3072
	ds_read_b128 v[132:135], v229
	ds_read_b128 v[136:139], v229 offset:1024
	ds_read_b128 v[140:143], v229 offset:2048
	ds_read_b128 v[144:147], v229 offset:3072
	ds_read_b128 v[188:191], v230
	ds_read_b128 v[192:195], v230 offset:1024
	ds_read_b128 v[180:183], v230 offset:2048
	ds_read_b128 v[184:187], v230 offset:3072
	ds_read_b128 v[172:175], v230 offset:4096
	ds_read_b128 v[176:179], v230 offset:5120
	ds_read_b128 v[164:167], v230 offset:6144
	ds_read_b128 v[168:171], v230 offset:7168
	s_and_b64 vcc, exec, s[74:75]
	s_cbranch_vccnz .Lrlx_0

; #define PG8_STAGE(bufoff, gbase, voff) do { _Pragma("unroll") for (int _i = 0; _i < 2; ++_i) \
;         __builtin_amdgcn_global_load_lds((const unsigned*)((const char*)(gbase) + (voff)[_i]), (PG8_LAS unsigned*)(lds + (bufoff) + ldsw + _i * 8192), 16, 0, 0); } while (0)
; #define PG8_LDA(dst, b, h) do { _Pragma("unroll") for (int m = 0; m < 4; ++m) _Pragma("unroll") for (int k = 0; k < 2; ++k) dst[m][k] = *(const PG8_LAS bf16x8*)(lds + PG8_SA(b, h) + aoff + m * 2048 + k * 1024); } while (0)
; #define PG8_LDB(dst, b, h) do { _Pragma("unroll") for (int n = 0; n < 2; ++n) _Pragma("unroll") for (int k = 0; k < 2; ++k) dst[n][k] = *(const PG8_LAS bf16x8*)(lds + PG8_SB(b, h) + boff + n * 2048 + k * 1024); } while (0)
; #define PG8_MMA(ai, bj, At, Bt) do { __builtin_amdgcn_s_setprio(1); _Pragma("unroll") for (int m = 0; m < 4; ++m) _Pragma("unroll") for (int n = 0; n < 2; ++n) _Pragma("unroll") for (int k = 0; k < 2; ++k) \
;         acc[ai][bj][m][n] = mma16(Bt[n][k], At[m][k], acc[ai][bj][m][n]); __builtin_amdgcn_s_setprio(0); } while (0)
; template <class Epi, class Sched, bool ALIGN_EPI = false, bool SP2 = false>
; __device__ __forceinline__ void gemm_phase(PG8_LAS unsigned char* lds, const Gemm g, const Sched& S, const Epi& E, Stopwatch& sw) {
;     ...
;             const bool last = (t == nt - 2);
;             const char* a1 = cA + (size_t)(t + 1) * kstep;
;             const char* a2 = last ? nA : cA + (size_t)(t + 2) * kstep; const char* b2 = last ? nB : cB + (size_t)(t + 2) * kstep;
;             const char* a3 = a2 + kstep; const char* b3 = b2 + kstep;
;             if (last && has_next) S.a_ready(nxt);
;             if constexpr (SP2) {
;             int relax = __builtin_amdgcn_readfirstlane((int)((ui > 0) && (t == 0))); asm volatile("" : "+s"(relax));
;             PG8_LDB(B0, 0, 0); PG8_LDB(B1, 0, 1); PG8_SCHED; PG8_LDA(At, 0, 0); if (!relax) PG8_STAGE(PG8_SA(1, 1), a1 + hstep, voffA);
;             if (relax) PG8_WAIT_VN(8 + Epi::NST); else PG8_WAIT_V(8); PG8_WAIT_L(0); PG8_BAR; PG8_MMA(0, 0, At, B0); PG8_MMA(0, 1, At, B1); PG8_BAR; PG8_SCHED;
;             PG8_LDA(At, 0, 1); PG8_STAGE(PG8_SB(0, 0), b2, voffB); PG8_STAGE(PG8_SB(0, 1), b2 + hstep, voffB); PG8_STAGE(PG8_SA(0, 0), a2, voffA);
;             if (relax) PG8_WAIT_VN(8 + Epi::NST); else PG8_WAIT_V(8); PG8_WAIT_L(0); PG8_BAR; PG8_MMA(1, 0, At, B0); PG8_MMA(1, 1, At, B1); PG8_BAR; PG8_SCHED;
.LBB0_157:
	s_add_u32 s38, s56, s60
	s_addc_u32 s39, s57, s61
	s_add_u32 s68, s38, 0x100
	s_addc_u32 s69, s39, 0
	s_add_u32 s62, s76, s60
	s_addc_u32 s63, s77, s61
	s_cmpk_eq_i32 s60, 0x700
	s_cselect_b64 s[64:65], -1, 0
	s_waitcnt lgkmcnt(0)
	s_and_b64 s[38:39], s[64:65], exec
	s_cselect_b32 s63, s49, s63
	s_cselect_b32 s62, s82, s62
	s_cselect_b32 s69, s3, s69
	s_cselect_b32 s68, s51, s68
	s_barrier
	s_setprio 1
	s_waitcnt lgkmcnt(0)
	v_mfma_i32_16x16x64_i8 v[128:131], v[148:151], v[188:191], v[128:131]
	v_mfma_i32_16x16x64_i8 v[124:127], v[156:159], v[188:191], v[124:127]
	v_mfma_i32_16x16x64_i8 v[120:123], v[148:151], v[180:183], v[120:123]
	v_mfma_i32_16x16x64_i8 v[116:119], v[156:159], v[180:183], v[116:119]
	v_mfma_i32_16x16x64_i8 v[112:115], v[148:151], v[172:175], v[112:115]
	v_mfma_i32_16x16x64_i8 v[108:111], v[156:159], v[172:175], v[108:111]
	v_mfma_i32_16x16x64_i8 v[104:107], v[148:151], v[164:167], v[104:107]
	v_mfma_i32_16x16x64_i8 v[100:103], v[156:159], v[164:167], v[100:103]
	v_mfma_i32_16x16x64_i8 v[128:131], v[152:155], v[192:195], v[128:131]
	v_mfma_i32_16x16x64_i8 v[124:127], v[160:163], v[192:195], v[124:127]
	v_mfma_i32_16x16x64_i8 v[120:123], v[152:155], v[184:187], v[120:123]
	v_mfma_i32_16x16x64_i8 v[116:119], v[160:163], v[184:187], v[116:119]
	v_mfma_i32_16x16x64_i8 v[112:115], v[152:155], v[176:179], v[112:115]
	v_mfma_i32_16x16x64_i8 v[108:111], v[160:163], v[176:179], v[108:111]
	v_mfma_i32_16x16x64_i8 v[104:107], v[152:155], v[168:171], v[104:107]
	v_mfma_i32_16x16x64_i8 v[100:103], v[160:163], v[168:171], v[100:103]
	v_mfma_i32_16x16x64_i8 v[72:75], v[132:135], v[188:191], v[72:75]
	v_mfma_i32_16x16x64_i8 v[68:71], v[140:143], v[188:191], v[68:71]
	v_mfma_i32_16x16x64_i8 v[64:67], v[132:135], v[180:183], v[64:67]
	v_mfma_i32_16x16x64_i8 v[60:63], v[140:143], v[180:183], v[60:63]
	v_mfma_i32_16x16x64_i8 v[56:59], v[132:135], v[172:175], v[56:59]
	v_mfma_i32_16x16x64_i8 v[52:55], v[140:143], v[172:175], v[52:55]
	v_mfma_i32_16x16x64_i8 v[48:51], v[132:135], v[164:167], v[48:51]
	v_mfma_i32_16x16x64_i8 v[44:47], v[140:143], v[164:167], v[44:47]
	v_mfma_i32_16x16x64_i8 v[72:75], v[136:139], v[192:195], v[72:75]
	v_mfma_i32_16x16x64_i8 v[68:71], v[144:147], v[192:195], v[68:71]
	v_mfma_i32_16x16x64_i8 v[64:67], v[136:139], v[184:187], v[64:67]
	v_mfma_i32_16x16x64_i8 v[60:63], v[144:147], v[184:187], v[60:63]
	v_mfma_i32_16x16x64_i8 v[56:59], v[136:139], v[176:179], v[56:59]
	v_mfma_i32_16x16x64_i8 v[52:55], v[144:147], v[176:179], v[52:55]
	v_mfma_i32_16x16x64_i8 v[48:51], v[136:139], v[168:171], v[48:51]
	v_mfma_i32_16x16x64_i8 v[44:47], v[144:147], v[168:171], v[44:47]
	s_setprio 0
	s_barrier
	s_mov_b32 m0, s18
	v_lshl_add_u64 v[218:219], s[62:63], 0, v[2:3]
	s_add_u32 s38, s62, 0x40000
	ds_read_b128 v[188:191], v230 offset:16384
	ds_read_b128 v[192:195], v230 offset:17408
	ds_read_b128 v[180:183], v230 offset:18432
	ds_read_b128 v[184:187], v230 offset:19456
	ds_read_b128 v[172:175], v230 offset:20480
	ds_read_b128 v[176:179], v230 offset:21504
	ds_read_b128 v[164:167], v230 offset:22528
	ds_read_b128 v[168:171], v230 offset:23552
	global_load_lds_dwordx4 v[218:219], off
	v_lshl_add_u64 v[220:221], s[62:63], 0, v[196:197]
	s_mov_b32 m0, s19
	s_addc_u32 s39, s63, 0
	global_load_lds_dwordx4 v[220:221], off
	v_lshl_add_u64 v[222:223], s[38:39], 0, v[2:3]
	s_mov_b32 m0, s16
	v_lshl_add_u64 v[224:225], s[68:69], 0, v[202:203]
	global_load_lds_dwordx4 v[222:223], off
	v_lshl_add_u64 v[222:223], s[38:39], 0, v[196:197]
	s_mov_b32 m0, s90
	v_cndmask_b32_e64 v231, 0, 1, s[74:75]
	global_load_lds_dwordx4 v[222:223], off
	v_lshl_add_u64 v[222:223], s[68:69], 0, v[204:205]
	s_mov_b32 m0, s81
	v_cmp_ne_u32_e64 s[38:39], 1, v231
	global_load_lds_dwordx4 v[222:223], off
	s_mov_b32 m0, s72
	s_andn2_b64 vcc, exec, s[74:75]
	global_load_lds_dwordx4 v[224:225], off
	s_cbranch_vccz .Lrlx_1

; #define PG8_STAGE(bufoff, gbase, voff) do { _Pragma("unroll") for (int _i = 0; _i < 2; ++_i) \
;         __builtin_amdgcn_global_load_lds((const unsigned*)((const char*)(gbase) + (voff)[_i]), (PG8_LAS unsigned*)(lds + (bufoff) + ldsw + _i * 8192), 16, 0, 0); } while (0)
; #define PG8_LDA(dst, b, h) do { _Pragma("unroll") for (int m = 0; m < 4; ++m) _Pragma("unroll") for (int k = 0; k < 2; ++k) dst[m][k] = *(const PG8_LAS bf16x8*)(lds + PG8_SA(b, h) + aoff + m * 2048 + k * 1024); } while (0)
; #define PG8_LDB(dst, b, h) do { _Pragma("unroll") for (int n = 0; n < 2; ++n) _Pragma("unroll") for (int k = 0; k < 2; ++k) dst[n][k] = *(const PG8_LAS bf16x8*)(lds + PG8_SB(b, h) + boff + n * 2048 + k * 1024); } while (0)
; #define PG8_MMA(ai, bj, At, Bt) do { __builtin_amdgcn_s_setprio(1); _Pragma("unroll") for (int m = 0; m < 4; ++m) _Pragma("unroll") for (int n = 0; n < 2; ++n) _Pragma("unroll") for (int k = 0; k < 2; ++k) \
;         acc[ai][bj][m][n] = mma16(Bt[n][k], At[m][k], acc[ai][bj][m][n]); __builtin_amdgcn_s_setprio(0); } while (0)
; #define PG8_WAIT_V(n) asm volatile("s_waitcnt vmcnt(" #n ")" ::: "memory")
; #define PG8_WAIT_VN(n) asm volatile("s_waitcnt vmcnt(%0)" :: "n"(n) : "memory")
; #define PG8_WAIT_L(n) asm volatile("s_waitcnt lgkmcnt(" #n ")" ::: "memory")
; #define PG8_BAR __builtin_amdgcn_s_barrier()
; #define PG8_SCHED __builtin_amdgcn_sched_barrier(0)
; template <class Epi, class Sched, bool ALIGN_EPI = false, bool SP2 = false>
; __device__ __forceinline__ void gemm_phase(PG8_LAS unsigned char* lds, const Gemm g, const Sched& S, const Epi& E, Stopwatch& sw) {
;     ...
;             if (relax) PG8_WAIT_VN(8 + Epi::NST); else PG8_WAIT_V(8); PG8_WAIT_L(0); PG8_BAR; PG8_MMA(1, 0, At, B0); PG8_MMA(1, 1, At, B1); PG8_BAR; PG8_SCHED;
;             PG8_LDB(B0, 1, 0); PG8_LDB(B1, 1, 1); PG8_SCHED; PG8_LDA(At, 1, 0); PG8_STAGE(PG8_SA(0, 1), a2 + hstep, voffA);
;             if (relax) PG8_WAIT_VN(8 + Epi::NST); else PG8_WAIT_V(8); PG8_WAIT_L(0); PG8_BAR; PG8_MMA(0, 0, At, B0); PG8_MMA(0, 1, At, B1); PG8_BAR; PG8_SCHED;
.LBB0_160:
	s_waitcnt lgkmcnt(0)
	s_barrier
	s_setprio 1
	s_waitcnt lgkmcnt(0)
	v_mfma_i32_16x16x64_i8 v[96:99], v[148:151], v[188:191], v[96:99]
	v_mfma_i32_16x16x64_i8 v[92:95], v[156:159], v[188:191], v[92:95]
	v_mfma_i32_16x16x64_i8 v[88:91], v[148:151], v[180:183], v[88:91]
	v_mfma_i32_16x16x64_i8 v[84:87], v[156:159], v[180:183], v[84:87]
	v_mfma_i32_16x16x64_i8 v[80:83], v[148:151], v[172:175], v[80:83]
	v_mfma_i32_16x16x64_i8 v[76:79], v[156:159], v[172:175], v[76:79]
	v_mfma_i32_16x16x64_i8 v[40:43], v[148:151], v[164:167], v[40:43]
	v_mfma_i32_16x16x64_i8 v[36:39], v[156:159], v[164:167], v[36:39]
	v_mfma_i32_16x16x64_i8 v[96:99], v[152:155], v[192:195], v[96:99]
	v_mfma_i32_16x16x64_i8 v[92:95], v[160:163], v[192:195], v[92:95]
	v_mfma_i32_16x16x64_i8 v[88:91], v[152:155], v[184:187], v[88:91]
	v_mfma_i32_16x16x64_i8 v[84:87], v[160:163], v[184:187], v[84:87]
	v_mfma_i32_16x16x64_i8 v[80:83], v[152:155], v[176:179], v[80:83]
	v_mfma_i32_16x16x64_i8 v[76:79], v[160:163], v[176:179], v[76:79]
	v_mfma_i32_16x16x64_i8 v[40:43], v[152:155], v[168:171], v[40:43]
	v_mfma_i32_16x16x64_i8 v[36:39], v[160:163], v[168:171], v[36:39]
	v_mfma_i32_16x16x64_i8 v[32:35], v[132:135], v[188:191], v[32:35]
	v_mfma_i32_16x16x64_i8 v[28:31], v[140:143], v[188:191], v[28:31]
	v_mfma_i32_16x16x64_i8 v[24:27], v[132:135], v[180:183], v[24:27]
	v_mfma_i32_16x16x64_i8 v[20:23], v[140:143], v[180:183], v[20:23]
	v_mfma_i32_16x16x64_i8 v[16:19], v[132:135], v[172:175], v[16:19]
	v_mfma_i32_16x16x64_i8 v[12:15], v[140:143], v[172:175], v[12:15]
	v_mfma_i32_16x16x64_i8 v[8:11], v[132:135], v[164:167], v[8:11]
	v_mfma_i32_16x16x64_i8 v[4:7], v[140:143], v[164:167], v[4:7]
	v_mfma_i32_16x16x64_i8 v[32:35], v[136:139], v[192:195], v[32:35]
	v_mfma_i32_16x16x64_i8 v[28:31], v[144:147], v[192:195], v[28:31]
	v_mfma_i32_16x16x64_i8 v[24:27], v[136:139], v[184:187], v[24:27]
	v_mfma_i32_16x16x64_i8 v[20:23], v[144:147], v[184:187], v[20:23]
	v_mfma_i32_16x16x64_i8 v[16:19], v[136:139], v[176:179], v[16:19]
	v_mfma_i32_16x16x64_i8 v[12:15], v[144:147], v[176:179], v[12:15]
	v_mfma_i32_16x16x64_i8 v[8:11], v[136:139], v[168:171], v[8:11]
	v_mfma_i32_16x16x64_i8 v[4:7], v[144:147], v[168:171], v[4:7]
	s_setprio 0
	s_barrier
	v_add_u32_e32 v132, 0x18000, v227
	v_add_u32_e32 v144, 0x1c000, v227
	ds_read_b128 v[148:151], v132
	ds_read_b128 v[152:155], v132 offset:1024
	ds_read_b128 v[156:159], v132 offset:2048
	ds_read_b128 v[160:163], v132 offset:3072
	ds_read_b128 v[132:135], v144
	ds_read_b128 v[136:139], v144 offset:1024
	ds_read_b128 v[140:143], v144 offset:2048
	ds_read_b128 v[144:147], v144 offset:3072
	s_add_u32 s68, s68, 0x40000
	s_addc_u32 s69, s69, 0
	s_mov_b32 m0, s73
	v_lshl_add_u64 v[232:233], s[68:69], 0, v[204:205]
	ds_read_b128 v[188:191], v230 offset:32768
	ds_read_b128 v[192:195], v230 offset:33792
	ds_read_b128 v[180:183], v230 offset:34816
	ds_read_b128 v[184:187], v230 offset:35840
	ds_read_b128 v[172:175], v230 offset:36864
	ds_read_b128 v[176:179], v230 offset:37888
	ds_read_b128 v[164:167], v230 offset:38912
	ds_read_b128 v[168:171], v230 offset:39936
	global_load_lds_dwordx4 v[232:233], off
	v_lshl_add_u64 v[232:233], s[68:69], 0, v[202:203]
	s_mov_b32 m0, s4
	s_and_b64 vcc, exec, s[38:39]
	global_load_lds_dwordx4 v[232:233], off
	s_mov_b64 s[74:75], s[10:11]
	s_cbranch_vccz .Lrlx_2

; #define PG8_STAGE(bufoff, gbase, voff) do { _Pragma("unroll") for (int _i = 0; _i < 2; ++_i) \
;         __builtin_amdgcn_global_load_lds((const unsigned*)((const char*)(gbase) + (voff)[_i]), (PG8_LAS unsigned*)(lds + (bufoff) + ldsw + _i * 8192), 16, 0, 0); } while (0)
; #define PG8_LDA(dst, b, h) do { _Pragma("unroll") for (int m = 0; m < 4; ++m) _Pragma("unroll") for (int k = 0; k < 2; ++k) dst[m][k] = *(const PG8_LAS bf16x8*)(lds + PG8_SA(b, h) + aoff + m * 2048 + k * 1024); } while (0)
; #define PG8_LDB(dst, b, h) do { _Pragma("unroll") for (int n = 0; n < 2; ++n) _Pragma("unroll") for (int k = 0; k < 2; ++k) dst[n][k] = *(const PG8_LAS bf16x8*)(lds + PG8_SB(b, h) + boff + n * 2048 + k * 1024); } while (0)
; #define PG8_MMA(ai, bj, At, Bt) do { __builtin_amdgcn_s_setprio(1); _Pragma("unroll") for (int m = 0; m < 4; ++m) _Pragma("unroll") for (int n = 0; n < 2; ++n) _Pragma("unroll") for (int k = 0; k < 2; ++k) \
;         acc[ai][bj][m][n] = mma16(Bt[n][k], At[m][k], acc[ai][bj][m][n]); __builtin_amdgcn_s_setprio(0); } while (0)
; #define PG8_WAIT_V(n) asm volatile("s_waitcnt vmcnt(" #n ")" ::: "memory")
; #define PG8_WAIT_VN(n) asm volatile("s_waitcnt vmcnt(%0)" :: "n"(n) : "memory")
; #define PG8_WAIT_L(n) asm volatile("s_waitcnt lgkmcnt(" #n ")" ::: "memory")
; #define PG8_BAR __builtin_amdgcn_s_barrier()
; #define PG8_SCHED __builtin_amdgcn_sched_barrier(0)
; template <class Epi, class Sched, bool ALIGN_EPI = false, bool SP2 = false>
; __device__ __forceinline__ void gemm_phase(PG8_LAS unsigned char* lds, const Gemm g, const Sched& S, const Epi& E, Stopwatch& sw) {
;     ...
;             PG8_LDB(B0, 0, 0); PG8_LDB(B1, 0, 1); PG8_SCHED; PG8_LDA(At, 0, 0); if (!relax) PG8_STAGE(PG8_SA(1, 1), a1 + hstep, voffA);
;             if (relax) PG8_WAIT_VN(8 + Epi::NST); else PG8_WAIT_V(8); PG8_WAIT_L(0); PG8_BAR; PG8_MMA(0, 0, At, B0); PG8_MMA(0, 1, At, B1); PG8_BAR; PG8_SCHED;
.Lrlx_0:
	s_waitcnt vmcnt(24)
	s_branch .LBB0_157

; #define PG8_STAGE(bufoff, gbase, voff) do { _Pragma("unroll") for (int _i = 0; _i < 2; ++_i) \
;         __builtin_amdgcn_global_load_lds((const unsigned*)((const char*)(gbase) + (voff)[_i]), (PG8_LAS unsigned*)(lds + (bufoff) + ldsw + _i * 8192), 16, 0, 0); } while (0)
; #define PG8_LDA(dst, b, h) do { _Pragma("unroll") for (int m = 0; m < 4; ++m) _Pragma("unroll") for (int k = 0; k < 2; ++k) dst[m][k] = *(const PG8_LAS bf16x8*)(lds + PG8_SA(b, h) + aoff + m * 2048 + k * 1024); } while (0)
; #define PG8_LDB(dst, b, h) do { _Pragma("unroll") for (int n = 0; n < 2; ++n) _Pragma("unroll") for (int k = 0; k < 2; ++k) dst[n][k] = *(const PG8_LAS bf16x8*)(lds + PG8_SB(b, h) + boff + n * 2048 + k * 1024); } while (0)
; #define PG8_MMA(ai, bj, At, Bt) do { __builtin_amdgcn_s_setprio(1); _Pragma("unroll") for (int m = 0; m < 4; ++m) _Pragma("unroll") for (int n = 0; n < 2; ++n) _Pragma("unroll") for (int k = 0; k < 2; ++k) \
;         acc[ai][bj][m][n] = mma16(Bt[n][k], At[m][k], acc[ai][bj][m][n]); __builtin_amdgcn_s_setprio(0); } while (0)
; #define PG8_WAIT_V(n) asm volatile("s_waitcnt vmcnt(" #n ")" ::: "memory")
; #define PG8_WAIT_VN(n) asm volatile("s_waitcnt vmcnt(%0)" :: "n"(n) : "memory")
; #define PG8_WAIT_L(n) asm volatile("s_waitcnt lgkmcnt(" #n ")" ::: "memory")
; #define PG8_BAR __builtin_amdgcn_s_barrier()
; #define PG8_SCHED __builtin_amdgcn_sched_barrier(0)
; template <class Epi, class Sched, bool ALIGN_EPI = false, bool SP2 = false>
; __device__ __forceinline__ void gemm_phase(PG8_LAS unsigned char* lds, const Gemm g, const Sched& S, const Epi& E, Stopwatch& sw) {
;     ...
;             int relax = __builtin_amdgcn_readfirstlane((int)((ui > 0) && (t == 0))); asm volatile("" : "+s"(relax));
;             PG8_LDB(B0, 0, 0); PG8_LDB(B1, 0, 1); PG8_SCHED; PG8_LDA(At, 0, 0); if (!relax) PG8_STAGE(PG8_SA(1, 1), a1 + hstep, voffA);
;             if (relax) PG8_WAIT_VN(8 + Epi::NST); else PG8_WAIT_V(8); PG8_WAIT_L(0); PG8_BAR; PG8_MMA(0, 0, At, B0); PG8_MMA(0, 1, At, B1); PG8_BAR; PG8_SCHED;
.LBB0_777:
	s_cmp_eq_u32 s58, 0
	s_cselect_b64 s[42:43], -1, 0
	s_and_b64 s[68:69], s[56:57], s[42:43]
	v_add_u32_e32 v2, 0x10000, v248
	ds_read_b128 v[150:153], v2
	ds_read_b128 v[154:157], v2 offset:1024
	ds_read_b128 v[158:161], v2 offset:2048
	ds_read_b128 v[162:165], v2 offset:3072
	v_add_u32_e32 v2, 0x14000, v248
	ds_read_b128 v[134:137], v2
	ds_read_b128 v[138:141], v2 offset:1024
	ds_read_b128 v[142:145], v2 offset:2048
	ds_read_b128 v[146:149], v2 offset:3072
	ds_read_b128 v[190:193], v249
	ds_read_b128 v[194:197], v249 offset:1024
	ds_read_b128 v[182:185], v249 offset:2048
	ds_read_b128 v[186:189], v249 offset:3072
	ds_read_b128 v[174:177], v249 offset:4096
	ds_read_b128 v[178:181], v249 offset:5120
	ds_read_b128 v[166:169], v249 offset:6144
	ds_read_b128 v[170:173], v249 offset:7168
	s_and_b64 vcc, exec, s[68:69]
	s_cbranch_vccnz .Lrlx_3

; #define PG8_STAGE(bufoff, gbase, voff) do { _Pragma("unroll") for (int _i = 0; _i < 2; ++_i) \
;         __builtin_amdgcn_global_load_lds((const unsigned*)((const char*)(gbase) + (voff)[_i]), (PG8_LAS unsigned*)(lds + (bufoff) + ldsw + _i * 8192), 16, 0, 0); } while (0)
; #define PG8_LDA(dst, b, h) do { _Pragma("unroll") for (int m = 0; m < 4; ++m) _Pragma("unroll") for (int k = 0; k < 2; ++k) dst[m][k] = *(const PG8_LAS bf16x8*)(lds + PG8_SA(b, h) + aoff + m * 2048 + k * 1024); } while (0)
; #define PG8_LDB(dst, b, h) do { _Pragma("unroll") for (int n = 0; n < 2; ++n) _Pragma("unroll") for (int k = 0; k < 2; ++k) dst[n][k] = *(const PG8_LAS bf16x8*)(lds + PG8_SB(b, h) + boff + n * 2048 + k * 1024); } while (0)
; #define PG8_MMA(ai, bj, At, Bt) do { __builtin_amdgcn_s_setprio(1); _Pragma("unroll") for (int m = 0; m < 4; ++m) _Pragma("unroll") for (int n = 0; n < 2; ++n) _Pragma("unroll") for (int k = 0; k < 2; ++k) \
;         acc[ai][bj][m][n] = mma16(Bt[n][k], At[m][k], acc[ai][bj][m][n]); __builtin_amdgcn_s_setprio(0); } while (0)
; template <class Epi, class Sched, bool ALIGN_EPI = false, bool SP2 = false>
; __device__ __forceinline__ void gemm_phase(PG8_LAS unsigned char* lds, const Gemm g, const Sched& S, const Epi& E, Stopwatch& sw) {
;     ...
;             const bool last = (t == nt - 2);
;             const char* a1 = cA + (size_t)(t + 1) * kstep;
;             const char* a2 = last ? nA : cA + (size_t)(t + 2) * kstep; const char* b2 = last ? nB : cB + (size_t)(t + 2) * kstep;
;             const char* a3 = a2 + kstep; const char* b3 = b2 + kstep;
;             if (last && has_next) S.a_ready(nxt);
;             if constexpr (SP2) {
;             int relax = __builtin_amdgcn_readfirstlane((int)((ui > 0) && (t == 0))); asm volatile("" : "+s"(relax));
;             PG8_LDB(B0, 0, 0); PG8_LDB(B1, 0, 1); PG8_SCHED; PG8_LDA(At, 0, 0); if (!relax) PG8_STAGE(PG8_SA(1, 1), a1 + hstep, voffA);
;             if (relax) PG8_WAIT_VN(8 + Epi::NST); else PG8_WAIT_V(8); PG8_WAIT_L(0); PG8_BAR; PG8_MMA(0, 0, At, B0); PG8_MMA(0, 1, At, B1); PG8_BAR; PG8_SCHED;
;             PG8_LDA(At, 0, 1); PG8_STAGE(PG8_SB(0, 0), b2, voffB); PG8_STAGE(PG8_SB(0, 1), b2 + hstep, voffB); PG8_STAGE(PG8_SA(0, 0), a2, voffA);
;             if (relax) PG8_WAIT_VN(8 + Epi::NST); else PG8_WAIT_V(8); PG8_WAIT_L(0); PG8_BAR; PG8_MMA(1, 0, At, B0); PG8_MMA(1, 1, At, B1); PG8_BAR; PG8_SCHED;
.LBB0_780:
	s_add_u32 s0, s54, s58
	s_addc_u32 s3, s55, s59
	s_add_u32 s0, s0, 0x100
	s_addc_u32 s3, s3, 0
	s_add_u32 s34, s24, s58
	s_addc_u32 s60, s83, s59
	s_cmpk_eq_i32 s58, 0x1700
	s_cselect_b64 s[62:63], -1, 0
	s_waitcnt lgkmcnt(0)
	s_and_b64 s[42:43], s[62:63], exec
	s_cselect_b32 s61, s53, s60
	s_cselect_b32 s60, s52, s34
	s_cselect_b32 s65, s51, s3
	s_cselect_b32 s64, s50, s0
	s_barrier
	s_setprio 1
	s_waitcnt lgkmcnt(0)
	v_mfma_f32_16x16x32_bf16 v[130:133], v[150:153], v[190:193], v[130:133]
	v_mfma_f32_16x16x32_bf16 v[126:129], v[158:161], v[190:193], v[126:129]
	v_mfma_f32_16x16x32_bf16 v[114:117], v[150:153], v[182:185], v[114:117]
	v_mfma_f32_16x16x32_bf16 v[110:113], v[158:161], v[182:185], v[110:113]
	v_mfma_f32_16x16x32_bf16 v[98:101], v[150:153], v[174:177], v[98:101]
	v_mfma_f32_16x16x32_bf16 v[94:97], v[158:161], v[174:177], v[94:97]
	v_mfma_f32_16x16x32_bf16 v[82:85], v[150:153], v[166:169], v[82:85]
	v_mfma_f32_16x16x32_bf16 v[78:81], v[158:161], v[166:169], v[78:81]
	v_mfma_f32_16x16x32_bf16 v[130:133], v[154:157], v[194:197], v[130:133]
	v_mfma_f32_16x16x32_bf16 v[126:129], v[162:165], v[194:197], v[126:129]
	v_mfma_f32_16x16x32_bf16 v[114:117], v[154:157], v[186:189], v[114:117]
	v_mfma_f32_16x16x32_bf16 v[110:113], v[162:165], v[186:189], v[110:113]
	v_mfma_f32_16x16x32_bf16 v[98:101], v[154:157], v[178:181], v[98:101]
	v_mfma_f32_16x16x32_bf16 v[94:97], v[162:165], v[178:181], v[94:97]
	v_mfma_f32_16x16x32_bf16 v[82:85], v[154:157], v[170:173], v[82:85]
	v_mfma_f32_16x16x32_bf16 v[78:81], v[162:165], v[170:173], v[78:81]
	v_mfma_f32_16x16x32_bf16 v[122:125], v[134:137], v[190:193], v[122:125]
	v_mfma_f32_16x16x32_bf16 v[118:121], v[142:145], v[190:193], v[118:121]
	v_mfma_f32_16x16x32_bf16 v[106:109], v[134:137], v[182:185], v[106:109]
	v_mfma_f32_16x16x32_bf16 v[102:105], v[142:145], v[182:185], v[102:105]
	v_mfma_f32_16x16x32_bf16 v[90:93], v[134:137], v[174:177], v[90:93]
	v_mfma_f32_16x16x32_bf16 v[86:89], v[142:145], v[174:177], v[86:89]
	v_mfma_f32_16x16x32_bf16 v[74:77], v[134:137], v[166:169], v[74:77]
	v_mfma_f32_16x16x32_bf16 v[70:73], v[142:145], v[166:169], v[70:73]
	v_mfma_f32_16x16x32_bf16 v[122:125], v[138:141], v[194:197], v[122:125]
	v_mfma_f32_16x16x32_bf16 v[118:121], v[146:149], v[194:197], v[118:121]
	v_mfma_f32_16x16x32_bf16 v[106:109], v[138:141], v[186:189], v[106:109]
	v_mfma_f32_16x16x32_bf16 v[102:105], v[146:149], v[186:189], v[102:105]
	v_mfma_f32_16x16x32_bf16 v[90:93], v[138:141], v[178:181], v[90:93]
	v_mfma_f32_16x16x32_bf16 v[86:89], v[146:149], v[178:181], v[86:89]
	v_mfma_f32_16x16x32_bf16 v[74:77], v[138:141], v[170:173], v[74:77]
	v_mfma_f32_16x16x32_bf16 v[70:73], v[146:149], v[170:173], v[70:73]
	s_setprio 0
	s_barrier
	s_mov_b32 m0, s19
	v_lshl_add_u64 v[230:231], s[60:61], 0, v[206:207]
	s_add_u32 s42, s60, 0xc0000
	ds_read_b128 v[190:193], v249 offset:16384
	ds_read_b128 v[194:197], v249 offset:17408
	ds_read_b128 v[182:185], v249 offset:18432
	ds_read_b128 v[186:189], v249 offset:19456
	ds_read_b128 v[174:177], v249 offset:20480
	ds_read_b128 v[178:181], v249 offset:21504
	ds_read_b128 v[166:169], v249 offset:22528
	ds_read_b128 v[170:173], v249 offset:23552
	global_load_lds_dwordx4 v[230:231], off
	v_lshl_add_u64 v[232:233], s[60:61], 0, v[202:203]
	s_mov_b32 m0, s25
	s_addc_u32 s43, s61, 0
	global_load_lds_dwordx4 v[232:233], off
	v_lshl_add_u64 v[4:5], s[42:43], 0, v[206:207]
	s_mov_b32 m0, s72
	v_lshl_add_u64 v[234:235], s[64:65], 0, v[208:209]
	global_load_lds_dwordx4 v[4:5], off
	v_lshl_add_u64 v[4:5], s[42:43], 0, v[202:203]
	s_mov_b32 m0, s73
	v_lshl_add_u64 v[236:237], s[64:65], 0, v[204:205]
	global_load_lds_dwordx4 v[4:5], off
	s_mov_b32 m0, s18
	v_cndmask_b32_e64 v2, 0, 1, s[68:69]
	global_load_lds_dwordx4 v[234:235], off
	s_mov_b32 m0, s74
	v_cmp_ne_u32_e64 s[42:43], 1, v2
	global_load_lds_dwordx4 v[236:237], off
	s_andn2_b64 vcc, exec, s[68:69]
	s_cbranch_vccz .Lrlx_4

; #define PG8_STAGE(bufoff, gbase, voff) do { _Pragma("unroll") for (int _i = 0; _i < 2; ++_i) \
;         __builtin_amdgcn_global_load_lds((const unsigned*)((const char*)(gbase) + (voff)[_i]), (PG8_LAS unsigned*)(lds + (bufoff) + ldsw + _i * 8192), 16, 0, 0); } while (0)
; #define PG8_LDA(dst, b, h) do { _Pragma("unroll") for (int m = 0; m < 4; ++m) _Pragma("unroll") for (int k = 0; k < 2; ++k) dst[m][k] = *(const PG8_LAS bf16x8*)(lds + PG8_SA(b, h) + aoff + m * 2048 + k * 1024); } while (0)
; #define PG8_LDB(dst, b, h) do { _Pragma("unroll") for (int n = 0; n < 2; ++n) _Pragma("unroll") for (int k = 0; k < 2; ++k) dst[n][k] = *(const PG8_LAS bf16x8*)(lds + PG8_SB(b, h) + boff + n * 2048 + k * 1024); } while (0)
; #define PG8_MMA(ai, bj, At, Bt) do { __builtin_amdgcn_s_setprio(1); _Pragma("unroll") for (int m = 0; m < 4; ++m) _Pragma("unroll") for (int n = 0; n < 2; ++n) _Pragma("unroll") for (int k = 0; k < 2; ++k) \
;         acc[ai][bj][m][n] = mma16(Bt[n][k], At[m][k], acc[ai][bj][m][n]); __builtin_amdgcn_s_setprio(0); } while (0)
; #define PG8_WAIT_V(n) asm volatile("s_waitcnt vmcnt(" #n ")" ::: "memory")
; #define PG8_WAIT_VN(n) asm volatile("s_waitcnt vmcnt(%0)" :: "n"(n) : "memory")
; #define PG8_WAIT_L(n) asm volatile("s_waitcnt lgkmcnt(" #n ")" ::: "memory")
; #define PG8_BAR __builtin_amdgcn_s_barrier()
; #define PG8_SCHED __builtin_amdgcn_sched_barrier(0)
; template <class Epi, class Sched, bool ALIGN_EPI = false, bool SP2 = false>
; __device__ __forceinline__ void gemm_phase(PG8_LAS unsigned char* lds, const Gemm g, const Sched& S, const Epi& E, Stopwatch& sw) {
;     ...
;             if (relax) PG8_WAIT_VN(8 + Epi::NST); else PG8_WAIT_V(8); PG8_WAIT_L(0); PG8_BAR; PG8_MMA(1, 0, At, B0); PG8_MMA(1, 1, At, B1); PG8_BAR; PG8_SCHED;
;             PG8_LDB(B0, 1, 0); PG8_LDB(B1, 1, 1); PG8_SCHED; PG8_LDA(At, 1, 0); PG8_STAGE(PG8_SA(0, 1), a2 + hstep, voffA);
;             if (relax) PG8_WAIT_VN(8 + Epi::NST); else PG8_WAIT_V(8); PG8_WAIT_L(0); PG8_BAR; PG8_MMA(0, 0, At, B0); PG8_MMA(0, 1, At, B1); PG8_BAR; PG8_SCHED;
.LBB0_783:
	s_waitcnt lgkmcnt(0)
	s_barrier
	s_setprio 1
	s_waitcnt lgkmcnt(0)
	v_mfma_f32_16x16x32_bf16 v[66:69], v[150:153], v[190:193], v[66:69]
	v_mfma_f32_16x16x32_bf16 v[62:65], v[158:161], v[190:193], v[62:65]
	v_mfma_f32_16x16x32_bf16 v[50:53], v[150:153], v[182:185], v[50:53]
	v_mfma_f32_16x16x32_bf16 v[46:49], v[158:161], v[182:185], v[46:49]
	v_mfma_f32_16x16x32_bf16 v[34:37], v[150:153], v[174:177], v[34:37]
	v_mfma_f32_16x16x32_bf16 v[30:33], v[158:161], v[174:177], v[30:33]
	v_mfma_f32_16x16x32_bf16 v[18:21], v[150:153], v[166:169], v[18:21]
	v_mfma_f32_16x16x32_bf16 v[14:17], v[158:161], v[166:169], v[14:17]
	v_mfma_f32_16x16x32_bf16 v[66:69], v[154:157], v[194:197], v[66:69]
	v_mfma_f32_16x16x32_bf16 v[62:65], v[162:165], v[194:197], v[62:65]
	v_mfma_f32_16x16x32_bf16 v[50:53], v[154:157], v[186:189], v[50:53]
	v_mfma_f32_16x16x32_bf16 v[46:49], v[162:165], v[186:189], v[46:49]
	v_mfma_f32_16x16x32_bf16 v[34:37], v[154:157], v[178:181], v[34:37]
	v_mfma_f32_16x16x32_bf16 v[30:33], v[162:165], v[178:181], v[30:33]
	v_mfma_f32_16x16x32_bf16 v[18:21], v[154:157], v[170:173], v[18:21]
	v_mfma_f32_16x16x32_bf16 v[14:17], v[162:165], v[170:173], v[14:17]
	v_mfma_f32_16x16x32_bf16 v[58:61], v[134:137], v[190:193], v[58:61]
	v_mfma_f32_16x16x32_bf16 v[54:57], v[142:145], v[190:193], v[54:57]
	v_mfma_f32_16x16x32_bf16 v[42:45], v[134:137], v[182:185], v[42:45]
	v_mfma_f32_16x16x32_bf16 v[38:41], v[142:145], v[182:185], v[38:41]
	v_mfma_f32_16x16x32_bf16 v[26:29], v[134:137], v[174:177], v[26:29]
	v_mfma_f32_16x16x32_bf16 v[22:25], v[142:145], v[174:177], v[22:25]
	v_mfma_f32_16x16x32_bf16 v[10:13], v[134:137], v[166:169], v[10:13]
	v_mfma_f32_16x16x32_bf16 v[4:7], v[142:145], v[166:169], v[6:9]
	v_mfma_f32_16x16x32_bf16 v[58:61], v[138:141], v[194:197], v[58:61]
	v_mfma_f32_16x16x32_bf16 v[54:57], v[146:149], v[194:197], v[54:57]
	v_mfma_f32_16x16x32_bf16 v[42:45], v[138:141], v[186:189], v[42:45]
	v_mfma_f32_16x16x32_bf16 v[38:41], v[146:149], v[186:189], v[38:41]
	v_mfma_f32_16x16x32_bf16 v[26:29], v[138:141], v[178:181], v[26:29]
	v_mfma_f32_16x16x32_bf16 v[22:25], v[146:149], v[178:181], v[22:25]
	v_mfma_f32_16x16x32_bf16 v[10:13], v[138:141], v[170:173], v[10:13]
	v_mfma_f32_16x16x32_bf16 v[4:7], v[146:149], v[170:173], v[4:7]
	s_setprio 0
	s_barrier
	v_add_u32_e32 v2, 0x18000, v248
	ds_read_b128 v[150:153], v2
	ds_read_b128 v[154:157], v2 offset:1024
	ds_read_b128 v[158:161], v2 offset:2048
	ds_read_b128 v[162:165], v2 offset:3072
	v_add_u32_e32 v2, 0x1c000, v248
	ds_read_b128 v[134:137], v2
	ds_read_b128 v[138:141], v2 offset:1024
	ds_read_b128 v[142:145], v2 offset:2048
	ds_read_b128 v[146:149], v2 offset:3072
	s_add_u32 s64, s64, 0xc0000
	s_addc_u32 s65, s65, 0
	s_mov_b32 m0, s75
	v_lshl_add_u64 v[8:9], s[64:65], 0, v[208:209]
	ds_read_b128 v[190:193], v249 offset:32768
	ds_read_b128 v[194:197], v249 offset:33792
	ds_read_b128 v[182:185], v249 offset:34816
	ds_read_b128 v[186:189], v249 offset:35840
	ds_read_b128 v[174:177], v249 offset:36864
	ds_read_b128 v[178:181], v249 offset:37888
	ds_read_b128 v[166:169], v249 offset:38912
	ds_read_b128 v[170:173], v249 offset:39936
	global_load_lds_dwordx4 v[8:9], off
	v_lshl_add_u64 v[8:9], s[64:65], 0, v[204:205]
	s_mov_b32 m0, s78
	s_and_b64 vcc, exec, s[42:43]
	global_load_lds_dwordx4 v[8:9], off
	s_cbranch_vccz .Lrlx_5

; #define PG8_STAGE(bufoff, gbase, voff) do { _Pragma("unroll") for (int _i = 0; _i < 2; ++_i) \
;         __builtin_amdgcn_global_load_lds((const unsigned*)((const char*)(gbase) + (voff)[_i]), (PG8_LAS unsigned*)(lds + (bufoff) + ldsw + _i * 8192), 16, 0, 0); } while (0)
; #define PG8_LDA(dst, b, h) do { _Pragma("unroll") for (int m = 0; m < 4; ++m) _Pragma("unroll") for (int k = 0; k < 2; ++k) dst[m][k] = *(const PG8_LAS bf16x8*)(lds + PG8_SA(b, h) + aoff + m * 2048 + k * 1024); } while (0)
; #define PG8_LDB(dst, b, h) do { _Pragma("unroll") for (int n = 0; n < 2; ++n) _Pragma("unroll") for (int k = 0; k < 2; ++k) dst[n][k] = *(const PG8_LAS bf16x8*)(lds + PG8_SB(b, h) + boff + n * 2048 + k * 1024); } while (0)
; #define PG8_MMA(ai, bj, At, Bt) do { __builtin_amdgcn_s_setprio(1); _Pragma("unroll") for (int m = 0; m < 4; ++m) _Pragma("unroll") for (int n = 0; n < 2; ++n) _Pragma("unroll") for (int k = 0; k < 2; ++k) \
;         acc[ai][bj][m][n] = mma16(Bt[n][k], At[m][k], acc[ai][bj][m][n]); __builtin_amdgcn_s_setprio(0); } while (0)
; #define PG8_WAIT_V(n) asm volatile("s_waitcnt vmcnt(" #n ")" ::: "memory")
; #define PG8_WAIT_VN(n) asm volatile("s_waitcnt vmcnt(%0)" :: "n"(n) : "memory")
; #define PG8_WAIT_L(n) asm volatile("s_waitcnt lgkmcnt(" #n ")" ::: "memory")
; #define PG8_BAR __builtin_amdgcn_s_barrier()
; #define PG8_SCHED __builtin_amdgcn_sched_barrier(0)
; template <class Epi, class Sched, bool ALIGN_EPI = false, bool SP2 = false>
; __device__ __forceinline__ void gemm_phase(PG8_LAS unsigned char* lds, const Gemm g, const Sched& S, const Epi& E, Stopwatch& sw) {
;     ...
;             int relax = __builtin_amdgcn_readfirstlane((int)((ui > 0) && (t == 0))); asm volatile("" : "+s"(relax));
;             PG8_LDB(B0, 0, 0); PG8_LDB(B1, 0, 1); PG8_SCHED; PG8_LDA(At, 0, 0); if (!relax) PG8_STAGE(PG8_SA(1, 1), a1 + hstep, voffA);
;             if (relax) PG8_WAIT_VN(8 + Epi::NST); else PG8_WAIT_V(8); PG8_WAIT_L(0); PG8_BAR; PG8_MMA(0, 0, At, B0); PG8_MMA(0, 1, At, B1); PG8_BAR; PG8_SCHED;
.LBB0_890:
	s_cmp_eq_u32 s62, 0
	s_cselect_b64 s[42:43], -1, 0
	s_and_b64 s[78:79], s[60:61], s[42:43]
	v_add_u32_e32 v144, 0x14000, v227
	v_add_u32_e32 v132, 0x10000, v227
	ds_read_b128 v[148:151], v132
	ds_read_b128 v[152:155], v132 offset:1024
	ds_read_b128 v[156:159], v132 offset:2048
	ds_read_b128 v[160:163], v132 offset:3072
	ds_read_b128 v[132:135], v144
	ds_read_b128 v[136:139], v144 offset:1024
	ds_read_b128 v[140:143], v144 offset:2048
	ds_read_b128 v[144:147], v144 offset:3072
	ds_read_b128 v[188:191], v228
	ds_read_b128 v[192:195], v228 offset:1024
	ds_read_b128 v[180:183], v228 offset:2048
	ds_read_b128 v[184:187], v228 offset:3072
	ds_read_b128 v[172:175], v228 offset:4096
	ds_read_b128 v[176:179], v228 offset:5120
	ds_read_b128 v[164:167], v228 offset:6144
	ds_read_b128 v[168:171], v228 offset:7168
	s_and_b64 vcc, exec, s[78:79]
	s_cbranch_vccnz .Lrlx_6

; #define PG8_STAGE(bufoff, gbase, voff) do { _Pragma("unroll") for (int _i = 0; _i < 2; ++_i) \
;         __builtin_amdgcn_global_load_lds((const unsigned*)((const char*)(gbase) + (voff)[_i]), (PG8_LAS unsigned*)(lds + (bufoff) + ldsw + _i * 8192), 16, 0, 0); } while (0)
; #define PG8_LDA(dst, b, h) do { _Pragma("unroll") for (int m = 0; m < 4; ++m) _Pragma("unroll") for (int k = 0; k < 2; ++k) dst[m][k] = *(const PG8_LAS bf16x8*)(lds + PG8_SA(b, h) + aoff + m * 2048 + k * 1024); } while (0)
; #define PG8_LDB(dst, b, h) do { _Pragma("unroll") for (int n = 0; n < 2; ++n) _Pragma("unroll") for (int k = 0; k < 2; ++k) dst[n][k] = *(const PG8_LAS bf16x8*)(lds + PG8_SB(b, h) + boff + n * 2048 + k * 1024); } while (0)
; #define PG8_MMA(ai, bj, At, Bt) do { __builtin_amdgcn_s_setprio(1); _Pragma("unroll") for (int m = 0; m < 4; ++m) _Pragma("unroll") for (int n = 0; n < 2; ++n) _Pragma("unroll") for (int k = 0; k < 2; ++k) \
;         acc[ai][bj][m][n] = mma16(Bt[n][k], At[m][k], acc[ai][bj][m][n]); __builtin_amdgcn_s_setprio(0); } while (0)
; template <class Epi, class Sched, bool ALIGN_EPI = false, bool SP2 = false>
; __device__ __forceinline__ void gemm_phase(PG8_LAS unsigned char* lds, const Gemm g, const Sched& S, const Epi& E, Stopwatch& sw) {
;     ...
;             const bool last = (t == nt - 2);
;             const char* a1 = cA + (size_t)(t + 1) * kstep;
;             const char* a2 = last ? nA : cA + (size_t)(t + 2) * kstep; const char* b2 = last ? nB : cB + (size_t)(t + 2) * kstep;
;             const char* a3 = a2 + kstep; const char* b3 = b2 + kstep;
;             if (last && has_next) S.a_ready(nxt);
;             if constexpr (SP2) {
;             int relax = __builtin_amdgcn_readfirstlane((int)((ui > 0) && (t == 0))); asm volatile("" : "+s"(relax));
;             PG8_LDB(B0, 0, 0); PG8_LDB(B1, 0, 1); PG8_SCHED; PG8_LDA(At, 0, 0); if (!relax) PG8_STAGE(PG8_SA(1, 1), a1 + hstep, voffA);
;             if (relax) PG8_WAIT_VN(8 + Epi::NST); else PG8_WAIT_V(8); PG8_WAIT_L(0); PG8_BAR; PG8_MMA(0, 0, At, B0); PG8_MMA(0, 1, At, B1); PG8_BAR; PG8_SCHED;
;             PG8_LDA(At, 0, 1); PG8_STAGE(PG8_SB(0, 0), b2, voffB); PG8_STAGE(PG8_SB(0, 1), b2 + hstep, voffB); PG8_STAGE(PG8_SA(0, 0), a2, voffA);
;             if (relax) PG8_WAIT_VN(8 + Epi::NST); else PG8_WAIT_V(8); PG8_WAIT_L(0); PG8_BAR; PG8_MMA(1, 0, At, B0); PG8_MMA(1, 1, At, B1); PG8_BAR; PG8_SCHED;
.LBB0_893:
	s_add_u32 s42, s58, s62
	s_addc_u32 s43, s59, s63
	s_add_u32 s74, s42, 0x100
	s_addc_u32 s75, s43, 0
	s_add_u32 s64, s76, s62
	s_addc_u32 s65, s77, s63
	s_cmpk_eq_i32 s62, 0xf00
	s_cselect_b64 s[68:69], -1, 0
	s_waitcnt lgkmcnt(0)
	s_and_b64 s[42:43], s[68:69], exec
	s_cselect_b32 s65, s51, s65
	s_cselect_b32 s64, s91, s64
	s_cselect_b32 s75, s53, s75
	s_cselect_b32 s74, s3, s74
	s_barrier
	s_setprio 1
	s_waitcnt lgkmcnt(0)
	v_mfma_f32_16x16x32_bf16 v[128:131], v[148:151], v[188:191], v[128:131]
	v_mfma_f32_16x16x32_bf16 v[124:127], v[156:159], v[188:191], v[124:127]
	v_mfma_f32_16x16x32_bf16 v[112:115], v[148:151], v[180:183], v[112:115]
	v_mfma_f32_16x16x32_bf16 v[108:111], v[156:159], v[180:183], v[108:111]
	v_mfma_f32_16x16x32_bf16 v[96:99], v[148:151], v[172:175], v[96:99]
	v_mfma_f32_16x16x32_bf16 v[92:95], v[156:159], v[172:175], v[92:95]
	v_mfma_f32_16x16x32_bf16 v[80:83], v[148:151], v[164:167], v[80:83]
	v_mfma_f32_16x16x32_bf16 v[76:79], v[156:159], v[164:167], v[76:79]
	v_mfma_f32_16x16x32_bf16 v[128:131], v[152:155], v[192:195], v[128:131]
	v_mfma_f32_16x16x32_bf16 v[124:127], v[160:163], v[192:195], v[124:127]
	v_mfma_f32_16x16x32_bf16 v[112:115], v[152:155], v[184:187], v[112:115]
	v_mfma_f32_16x16x32_bf16 v[108:111], v[160:163], v[184:187], v[108:111]
	v_mfma_f32_16x16x32_bf16 v[96:99], v[152:155], v[176:179], v[96:99]
	v_mfma_f32_16x16x32_bf16 v[92:95], v[160:163], v[176:179], v[92:95]
	v_mfma_f32_16x16x32_bf16 v[80:83], v[152:155], v[168:171], v[80:83]
	v_mfma_f32_16x16x32_bf16 v[76:79], v[160:163], v[168:171], v[76:79]
	v_mfma_f32_16x16x32_bf16 v[120:123], v[132:135], v[188:191], v[120:123]
	v_mfma_f32_16x16x32_bf16 v[116:119], v[140:143], v[188:191], v[116:119]
	v_mfma_f32_16x16x32_bf16 v[104:107], v[132:135], v[180:183], v[104:107]
	v_mfma_f32_16x16x32_bf16 v[100:103], v[140:143], v[180:183], v[100:103]
	v_mfma_f32_16x16x32_bf16 v[88:91], v[132:135], v[172:175], v[88:91]
	v_mfma_f32_16x16x32_bf16 v[84:87], v[140:143], v[172:175], v[84:87]
	v_mfma_f32_16x16x32_bf16 v[72:75], v[132:135], v[164:167], v[72:75]
	v_mfma_f32_16x16x32_bf16 v[68:71], v[140:143], v[164:167], v[68:71]
	v_mfma_f32_16x16x32_bf16 v[120:123], v[136:139], v[192:195], v[120:123]
	v_mfma_f32_16x16x32_bf16 v[116:119], v[144:147], v[192:195], v[116:119]
	v_mfma_f32_16x16x32_bf16 v[104:107], v[136:139], v[184:187], v[104:107]
	v_mfma_f32_16x16x32_bf16 v[100:103], v[144:147], v[184:187], v[100:103]
	v_mfma_f32_16x16x32_bf16 v[88:91], v[136:139], v[176:179], v[88:91]
	v_mfma_f32_16x16x32_bf16 v[84:87], v[144:147], v[176:179], v[84:87]
	v_mfma_f32_16x16x32_bf16 v[72:75], v[136:139], v[168:171], v[72:75]
	v_mfma_f32_16x16x32_bf16 v[68:71], v[144:147], v[168:171], v[68:71]
	s_setprio 0
	s_barrier
	s_mov_b32 m0, s18
	v_lshl_add_u64 v[218:219], s[64:65], 0, v[2:3]
	s_add_u32 s42, s64, 0x80000
	ds_read_b128 v[188:191], v228 offset:16384
	ds_read_b128 v[192:195], v228 offset:17408
	ds_read_b128 v[180:183], v228 offset:18432
	ds_read_b128 v[184:187], v228 offset:19456
	ds_read_b128 v[172:175], v228 offset:20480
	ds_read_b128 v[176:179], v228 offset:21504
	ds_read_b128 v[164:167], v228 offset:22528
	ds_read_b128 v[168:171], v228 offset:23552
	global_load_lds_dwordx4 v[218:219], off
	v_lshl_add_u64 v[220:221], s[64:65], 0, v[196:197]
	s_mov_b32 m0, s19
	s_addc_u32 s43, s65, 0
	global_load_lds_dwordx4 v[220:221], off
	v_lshl_add_u64 v[222:223], s[42:43], 0, v[2:3]
	s_mov_b32 m0, s24
	v_lshl_add_u64 v[224:225], s[74:75], 0, v[202:203]
	global_load_lds_dwordx4 v[222:223], off
	v_lshl_add_u64 v[222:223], s[42:43], 0, v[196:197]
	s_mov_b32 m0, s25
	v_cndmask_b32_e64 v229, 0, 1, s[78:79]
	global_load_lds_dwordx4 v[222:223], off
	v_lshl_add_u64 v[222:223], s[74:75], 0, v[204:205]
	s_mov_b32 m0, s16
	v_cmp_ne_u32_e64 s[42:43], 1, v229
	global_load_lds_dwordx4 v[222:223], off
	s_mov_b32 m0, s31
	s_andn2_b64 vcc, exec, s[78:79]
	global_load_lds_dwordx4 v[224:225], off
	s_cbranch_vccz .Lrlx_7

; #define PG8_STAGE(bufoff, gbase, voff) do { _Pragma("unroll") for (int _i = 0; _i < 2; ++_i) \
;         __builtin_amdgcn_global_load_lds((const unsigned*)((const char*)(gbase) + (voff)[_i]), (PG8_LAS unsigned*)(lds + (bufoff) + ldsw + _i * 8192), 16, 0, 0); } while (0)
; #define PG8_LDA(dst, b, h) do { _Pragma("unroll") for (int m = 0; m < 4; ++m) _Pragma("unroll") for (int k = 0; k < 2; ++k) dst[m][k] = *(const PG8_LAS bf16x8*)(lds + PG8_SA(b, h) + aoff + m * 2048 + k * 1024); } while (0)
; #define PG8_LDB(dst, b, h) do { _Pragma("unroll") for (int n = 0; n < 2; ++n) _Pragma("unroll") for (int k = 0; k < 2; ++k) dst[n][k] = *(const PG8_LAS bf16x8*)(lds + PG8_SB(b, h) + boff + n * 2048 + k * 1024); } while (0)
; #define PG8_MMA(ai, bj, At, Bt) do { __builtin_amdgcn_s_setprio(1); _Pragma("unroll") for (int m = 0; m < 4; ++m) _Pragma("unroll") for (int n = 0; n < 2; ++n) _Pragma("unroll") for (int k = 0; k < 2; ++k) \
;         acc[ai][bj][m][n] = mma16(Bt[n][k], At[m][k], acc[ai][bj][m][n]); __builtin_amdgcn_s_setprio(0); } while (0)
; #define PG8_WAIT_V(n) asm volatile("s_waitcnt vmcnt(" #n ")" ::: "memory")
; #define PG8_WAIT_VN(n) asm volatile("s_waitcnt vmcnt(%0)" :: "n"(n) : "memory")
; #define PG8_WAIT_L(n) asm volatile("s_waitcnt lgkmcnt(" #n ")" ::: "memory")
; #define PG8_BAR __builtin_amdgcn_s_barrier()
; #define PG8_SCHED __builtin_amdgcn_sched_barrier(0)
; template <class Epi, class Sched, bool ALIGN_EPI = false, bool SP2 = false>
; __device__ __forceinline__ void gemm_phase(PG8_LAS unsigned char* lds, const Gemm g, const Sched& S, const Epi& E, Stopwatch& sw) {
;     ...
;             PG8_LDB(B0, 0, 0); PG8_LDB(B1, 0, 1); PG8_SCHED; PG8_LDA(At, 0, 0); if (!relax) PG8_STAGE(PG8_SA(1, 1), a1 + hstep, voffA);
;             if (relax) PG8_WAIT_VN(8 + Epi::NST); else PG8_WAIT_V(8); PG8_WAIT_L(0); PG8_BAR; PG8_MMA(0, 0, At, B0); PG8_MMA(0, 1, At, B1); PG8_BAR; PG8_SCHED;
.Lrlx_6:
	s_waitcnt vmcnt(32)
	s_branch .LBB0_893

; #define PG8_STAGE(bufoff, gbase, voff) do { _Pragma("unroll") for (int _i = 0; _i < 2; ++_i) \
;         __builtin_amdgcn_global_load_lds((const unsigned*)((const char*)(gbase) + (voff)[_i]), (PG8_LAS unsigned*)(lds + (bufoff) + ldsw + _i * 8192), 16, 0, 0); } while (0)
; #define PG8_LDA(dst, b, h) do { _Pragma("unroll") for (int m = 0; m < 4; ++m) _Pragma("unroll") for (int k = 0; k < 2; ++k) dst[m][k] = *(const PG8_LAS bf16x8*)(lds + PG8_SA(b, h) + aoff + m * 2048 + k * 1024); } while (0)
; #define PG8_LDB(dst, b, h) do { _Pragma("unroll") for (int n = 0; n < 2; ++n) _Pragma("unroll") for (int k = 0; k < 2; ++k) dst[n][k] = *(const PG8_LAS bf16x8*)(lds + PG8_SB(b, h) + boff + n * 2048 + k * 1024); } while (0)
; #define PG8_MMA(ai, bj, At, Bt) do { __builtin_amdgcn_s_setprio(1); _Pragma("unroll") for (int m = 0; m < 4; ++m) _Pragma("unroll") for (int n = 0; n < 2; ++n) _Pragma("unroll") for (int k = 0; k < 2; ++k) \
;         acc[ai][bj][m][n] = mma16(Bt[n][k], At[m][k], acc[ai][bj][m][n]); __builtin_amdgcn_s_setprio(0); } while (0)
; #define PG8_WAIT_V(n) asm volatile("s_waitcnt vmcnt(" #n ")" ::: "memory")
; #define PG8_WAIT_VN(n) asm volatile("s_waitcnt vmcnt(%0)" :: "n"(n) : "memory")
; #define PG8_WAIT_L(n) asm volatile("s_waitcnt lgkmcnt(" #n ")" ::: "memory")
; #define PG8_BAR __builtin_amdgcn_s_barrier()
; #define PG8_SCHED __builtin_amdgcn_sched_barrier(0)
; template <class Epi, class Sched, bool ALIGN_EPI = false, bool SP2 = false>
; __device__ __forceinline__ void gemm_phase(PG8_LAS unsigned char* lds, const Gemm g, const Sched& S, const Epi& E, Stopwatch& sw) {
;     ...
;             int relax = __builtin_amdgcn_readfirstlane((int)((ui > 0) && (t == 0))); asm volatile("" : "+s"(relax));
;             PG8_LDB(B0, 0, 0); PG8_LDB(B1, 0, 1); PG8_SCHED; PG8_LDA(At, 0, 0); if (!relax) PG8_STAGE(PG8_SA(1, 1), a1 + hstep, voffA);
;             if (relax) PG8_WAIT_VN(8 + Epi::NST); else PG8_WAIT_V(8); PG8_WAIT_L(0); PG8_BAR; PG8_MMA(0, 0, At, B0); PG8_MMA(0, 1, At, B1); PG8_BAR; PG8_SCHED;
.LBB0_1118:
	s_cmp_eq_u32 s62, 0
	s_cselect_b64 s[40:41], -1, 0
	s_and_b64 s[78:79], s[60:61], s[40:41]
	v_add_u32_e32 v144, 0x11000, v227
	v_add_u32_e32 v132, 0x10000, v227
	ds_read_b128 v[148:151], v132
	ds_read_b128 v[152:155], v132 offset:1024
	ds_read_b128 v[156:159], v132 offset:2048
	ds_read_b128 v[160:163], v132 offset:3072
	ds_read_b128 v[132:135], v144
	ds_read_b128 v[136:139], v144 offset:1024
	ds_read_b128 v[140:143], v144 offset:2048
	ds_read_b128 v[144:147], v144 offset:3072
	ds_read_b128 v[188:191], v228
	ds_read_b128 v[192:195], v228 offset:1024
	ds_read_b128 v[180:183], v228 offset:2048
	ds_read_b128 v[184:187], v228 offset:3072
	ds_read_b128 v[172:175], v228 offset:4096
	ds_read_b128 v[176:179], v228 offset:5120
	ds_read_b128 v[164:167], v228 offset:6144
	ds_read_b128 v[168:171], v228 offset:7168
	s_and_b64 vcc, exec, s[78:79]
	s_cbranch_vccnz .Lrlx_8

; #define PG8_STAGE(bufoff, gbase, voff) do { _Pragma("unroll") for (int _i = 0; _i < 2; ++_i) \
;         __builtin_amdgcn_global_load_lds((const unsigned*)((const char*)(gbase) + (voff)[_i]), (PG8_LAS unsigned*)(lds + (bufoff) + ldsw + _i * 8192), 16, 0, 0); } while (0)
; #define PG8_LDA(dst, b, h) do { _Pragma("unroll") for (int m = 0; m < 4; ++m) _Pragma("unroll") for (int k = 0; k < 2; ++k) dst[m][k] = *(const PG8_LAS bf16x8*)(lds + PG8_SA(b, h) + aoff + m * 2048 + k * 1024); } while (0)
; #define PG8_LDB(dst, b, h) do { _Pragma("unroll") for (int n = 0; n < 2; ++n) _Pragma("unroll") for (int k = 0; k < 2; ++k) dst[n][k] = *(const PG8_LAS bf16x8*)(lds + PG8_SB(b, h) + boff + n * 2048 + k * 1024); } while (0)
; #define PG8_MMA(ai, bj, At, Bt) do { __builtin_amdgcn_s_setprio(1); _Pragma("unroll") for (int m = 0; m < 4; ++m) _Pragma("unroll") for (int n = 0; n < 2; ++n) _Pragma("unroll") for (int k = 0; k < 2; ++k) \
;         acc[ai][bj][m][n] = mma16(Bt[n][k], At[m][k], acc[ai][bj][m][n]); __builtin_amdgcn_s_setprio(0); } while (0)
; template <class Epi, class Sched, bool ALIGN_EPI = false, bool SP2 = false>
; __device__ __forceinline__ void gemm_phase(PG8_LAS unsigned char* lds, const Gemm g, const Sched& S, const Epi& E, Stopwatch& sw) {
;     ...
;             const bool last = (t == nt - 2);
;             const char* a1 = cA + (size_t)(t + 1) * kstep;
;             const char* a2 = last ? nA : cA + (size_t)(t + 2) * kstep; const char* b2 = last ? nB : cB + (size_t)(t + 2) * kstep;
;             const char* a3 = a2 + kstep; const char* b3 = b2 + kstep;
;             if (last && has_next) S.a_ready(nxt);
;             if constexpr (SP2) {
;             int relax = __builtin_amdgcn_readfirstlane((int)((ui > 0) && (t == 0))); asm volatile("" : "+s"(relax));
;             PG8_LDB(B0, 0, 0); PG8_LDB(B1, 0, 1); PG8_SCHED; PG8_LDA(At, 0, 0); if (!relax) PG8_STAGE(PG8_SA(1, 1), a1 + hstep, voffA);
;             if (relax) PG8_WAIT_VN(8 + Epi::NST); else PG8_WAIT_V(8); PG8_WAIT_L(0); PG8_BAR; PG8_MMA(0, 0, At, B0); PG8_MMA(0, 1, At, B1); PG8_BAR; PG8_SCHED;
;             PG8_LDA(At, 0, 1); PG8_STAGE(PG8_SB(0, 0), b2, voffB); PG8_STAGE(PG8_SB(0, 1), b2 + hstep, voffB); PG8_STAGE(PG8_SA(0, 0), a2, voffA);
;             if (relax) PG8_WAIT_VN(8 + Epi::NST); else PG8_WAIT_V(8); PG8_WAIT_L(0); PG8_BAR; PG8_MMA(1, 0, At, B0); PG8_MMA(1, 1, At, B1); PG8_BAR; PG8_SCHED;
.LBB0_1121:
	s_add_u32 s40, s58, s62
	s_addc_u32 s41, s59, s63
	s_add_u32 s74, s40, 0x100
	s_addc_u32 s75, s41, 0
	s_add_u32 s64, s76, s62
	s_addc_u32 s65, s77, s63
	s_cmpk_eq_i32 s62, 0x700
	s_cselect_b64 s[68:69], -1, 0
	s_waitcnt lgkmcnt(0)
	s_and_b64 s[40:41], s[68:69], exec
	s_cselect_b32 s65, s51, s65
	s_cselect_b32 s64, s91, s64
	s_cselect_b32 s75, s53, s75
	s_cselect_b32 s74, s3, s74
	s_barrier
	s_setprio 1
	s_waitcnt lgkmcnt(0)
	v_mfma_i32_16x16x64_i8 v[128:131], v[148:151], v[188:191], v[128:131]
	v_mfma_i32_16x16x64_i8 v[124:127], v[156:159], v[188:191], v[124:127]
	v_mfma_i32_16x16x64_i8 v[120:123], v[148:151], v[180:183], v[120:123]
	v_mfma_i32_16x16x64_i8 v[116:119], v[156:159], v[180:183], v[116:119]
	v_mfma_i32_16x16x64_i8 v[112:115], v[148:151], v[172:175], v[112:115]
	v_mfma_i32_16x16x64_i8 v[108:111], v[156:159], v[172:175], v[108:111]
	v_mfma_i32_16x16x64_i8 v[104:107], v[148:151], v[164:167], v[104:107]
	v_mfma_i32_16x16x64_i8 v[100:103], v[156:159], v[164:167], v[100:103]
	v_mfma_i32_16x16x64_i8 v[128:131], v[152:155], v[192:195], v[128:131]
	v_mfma_i32_16x16x64_i8 v[124:127], v[160:163], v[192:195], v[124:127]
	v_mfma_i32_16x16x64_i8 v[120:123], v[152:155], v[184:187], v[120:123]
	v_mfma_i32_16x16x64_i8 v[116:119], v[160:163], v[184:187], v[116:119]
	v_mfma_i32_16x16x64_i8 v[112:115], v[152:155], v[176:179], v[112:115]
	v_mfma_i32_16x16x64_i8 v[108:111], v[160:163], v[176:179], v[108:111]
	v_mfma_i32_16x16x64_i8 v[104:107], v[152:155], v[168:171], v[104:107]
	v_mfma_i32_16x16x64_i8 v[100:103], v[160:163], v[168:171], v[100:103]
	v_mfma_i32_16x16x64_i8 v[76:79], v[132:135], v[188:191], v[76:79]
	v_mfma_i32_16x16x64_i8 v[68:71], v[140:143], v[188:191], v[68:71]
	v_mfma_i32_16x16x64_i8 v[60:63], v[132:135], v[180:183], v[60:63]
	v_mfma_i32_16x16x64_i8 v[52:55], v[140:143], v[180:183], v[52:55]
	v_mfma_i32_16x16x64_i8 v[48:51], v[132:135], v[172:175], v[48:51]
	v_mfma_i32_16x16x64_i8 v[44:47], v[140:143], v[172:175], v[44:47]
	v_mfma_i32_16x16x64_i8 v[40:43], v[132:135], v[164:167], v[40:43]
	v_mfma_i32_16x16x64_i8 v[36:39], v[140:143], v[164:167], v[36:39]
	v_mfma_i32_16x16x64_i8 v[76:79], v[136:139], v[192:195], v[76:79]
	v_mfma_i32_16x16x64_i8 v[68:71], v[144:147], v[192:195], v[68:71]
	v_mfma_i32_16x16x64_i8 v[60:63], v[136:139], v[184:187], v[60:63]
	v_mfma_i32_16x16x64_i8 v[52:55], v[144:147], v[184:187], v[52:55]
	v_mfma_i32_16x16x64_i8 v[48:51], v[136:139], v[176:179], v[48:51]
	v_mfma_i32_16x16x64_i8 v[44:47], v[144:147], v[176:179], v[44:47]
	v_mfma_i32_16x16x64_i8 v[40:43], v[136:139], v[168:171], v[40:43]
	v_mfma_i32_16x16x64_i8 v[36:39], v[144:147], v[168:171], v[36:39]
	s_setprio 0
	s_barrier
	s_mov_b32 m0, s25
	v_lshl_add_u64 v[218:219], s[64:65], 0, v[2:3]
	s_add_u32 s40, s64, 0x40000
	ds_read_b128 v[188:191], v228 offset:16384
	ds_read_b128 v[192:195], v228 offset:17408
	ds_read_b128 v[180:183], v228 offset:18432
	ds_read_b128 v[184:187], v228 offset:19456
	ds_read_b128 v[172:175], v228 offset:20480
	ds_read_b128 v[176:179], v228 offset:21504
	ds_read_b128 v[164:167], v228 offset:22528
	ds_read_b128 v[168:171], v228 offset:23552
	global_load_lds_dwordx4 v[218:219], off
	v_lshl_add_u64 v[220:221], s[64:65], 0, v[196:197]
	s_mov_b32 m0, s36
	s_addc_u32 s41, s65, 0
	global_load_lds_dwordx4 v[220:221], off
	v_lshl_add_u64 v[222:223], s[40:41], 0, v[2:3]
	s_mov_b32 m0, s37
	v_lshl_add_u64 v[224:225], s[74:75], 0, v[202:203]
	global_load_lds_dwordx4 v[222:223], off
	v_lshl_add_u64 v[222:223], s[40:41], 0, v[196:197]
	s_mov_b32 m0, s72
	v_cndmask_b32_e64 v229, 0, 1, s[78:79]
	global_load_lds_dwordx4 v[222:223], off
	v_lshl_add_u64 v[222:223], s[74:75], 0, v[204:205]
	s_mov_b32 m0, s19
	v_cmp_ne_u32_e64 s[40:41], 1, v229
	global_load_lds_dwordx4 v[222:223], off
	s_mov_b32 m0, s73
	s_andn2_b64 vcc, exec, s[78:79]
	global_load_lds_dwordx4 v[224:225], off
	s_cbranch_vccz .Lrlx_9

; #define PG8_STAGE(bufoff, gbase, voff) do { _Pragma("unroll") for (int _i = 0; _i < 2; ++_i) \
;         __builtin_amdgcn_global_load_lds((const unsigned*)((const char*)(gbase) + (voff)[_i]), (PG8_LAS unsigned*)(lds + (bufoff) + ldsw + _i * 8192), 16, 0, 0); } while (0)
; #define PG8_LDA(dst, b, h) do { _Pragma("unroll") for (int m = 0; m < 4; ++m) _Pragma("unroll") for (int k = 0; k < 2; ++k) dst[m][k] = *(const PG8_LAS bf16x8*)(lds + PG8_SA(b, h) + aoff + m * 2048 + k * 1024); } while (0)
; #define PG8_LDB(dst, b, h) do { _Pragma("unroll") for (int n = 0; n < 2; ++n) _Pragma("unroll") for (int k = 0; k < 2; ++k) dst[n][k] = *(const PG8_LAS bf16x8*)(lds + PG8_SB(b, h) + boff + n * 2048 + k * 1024); } while (0)
; #define PG8_MMA(ai, bj, At, Bt) do { __builtin_amdgcn_s_setprio(1); _Pragma("unroll") for (int m = 0; m < 4; ++m) _Pragma("unroll") for (int n = 0; n < 2; ++n) _Pragma("unroll") for (int k = 0; k < 2; ++k) \
;         acc[ai][bj][m][n] = mma16(Bt[n][k], At[m][k], acc[ai][bj][m][n]); __builtin_amdgcn_s_setprio(0); } while (0)
; #define PG8_WAIT_V(n) asm volatile("s_waitcnt vmcnt(" #n ")" ::: "memory")
; #define PG8_WAIT_VN(n) asm volatile("s_waitcnt vmcnt(%0)" :: "n"(n) : "memory")
; #define PG8_WAIT_L(n) asm volatile("s_waitcnt lgkmcnt(" #n ")" ::: "memory")
; #define PG8_BAR __builtin_amdgcn_s_barrier()
; #define PG8_SCHED __builtin_amdgcn_sched_barrier(0)
; template <class Epi, class Sched, bool ALIGN_EPI = false, bool SP2 = false>
; __device__ __forceinline__ void gemm_phase(PG8_LAS unsigned char* lds, const Gemm g, const Sched& S, const Epi& E, Stopwatch& sw) {
;     ...
;             int relax = __builtin_amdgcn_readfirstlane((int)((ui > 0) && (t == 0))); asm volatile("" : "+s"(relax));
;             PG8_LDB(B0, 0, 0); PG8_LDB(B1, 0, 1); PG8_SCHED; PG8_LDA(At, 0, 0); if (!relax) PG8_STAGE(PG8_SA(1, 1), a1 + hstep, voffA);
;             if (relax) PG8_WAIT_VN(8 + Epi::NST); else PG8_WAIT_V(8); PG8_WAIT_L(0); PG8_BAR; PG8_MMA(0, 0, At, B0); PG8_MMA(0, 1, At, B1); PG8_BAR; PG8_SCHED;
.LBB0_1228:
	s_cmp_eq_u32 s60, 0
	s_cselect_b64 s[40:41], -1, 0
	s_and_b64 s[74:75], s[58:59], s[40:41]
	v_add_u32_e32 v144, 0x14000, v227
	v_add_u32_e32 v132, 0x10000, v227
	ds_read_b128 v[148:151], v132
	ds_read_b128 v[152:155], v132 offset:1024
	ds_read_b128 v[156:159], v132 offset:2048
	ds_read_b128 v[160:163], v132 offset:3072
	ds_read_b128 v[132:135], v144
	ds_read_b128 v[136:139], v144 offset:1024
	ds_read_b128 v[140:143], v144 offset:2048
	ds_read_b128 v[144:147], v144 offset:3072
	ds_read_b128 v[188:191], v228
	ds_read_b128 v[192:195], v228 offset:1024
	ds_read_b128 v[180:183], v228 offset:2048
	ds_read_b128 v[184:187], v228 offset:3072
	ds_read_b128 v[172:175], v228 offset:4096
	ds_read_b128 v[176:179], v228 offset:5120
	ds_read_b128 v[164:167], v228 offset:6144
	ds_read_b128 v[168:171], v228 offset:7168
	s_and_b64 vcc, exec, s[74:75]
	s_cbranch_vccnz .Lrlx_10

; #define PG8_STAGE(bufoff, gbase, voff) do { _Pragma("unroll") for (int _i = 0; _i < 2; ++_i) \
;         __builtin_amdgcn_global_load_lds((const unsigned*)((const char*)(gbase) + (voff)[_i]), (PG8_LAS unsigned*)(lds + (bufoff) + ldsw + _i * 8192), 16, 0, 0); } while (0)
; #define PG8_LDA(dst, b, h) do { _Pragma("unroll") for (int m = 0; m < 4; ++m) _Pragma("unroll") for (int k = 0; k < 2; ++k) dst[m][k] = *(const PG8_LAS bf16x8*)(lds + PG8_SA(b, h) + aoff + m * 2048 + k * 1024); } while (0)
; #define PG8_LDB(dst, b, h) do { _Pragma("unroll") for (int n = 0; n < 2; ++n) _Pragma("unroll") for (int k = 0; k < 2; ++k) dst[n][k] = *(const PG8_LAS bf16x8*)(lds + PG8_SB(b, h) + boff + n * 2048 + k * 1024); } while (0)
; #define PG8_MMA(ai, bj, At, Bt) do { __builtin_amdgcn_s_setprio(1); _Pragma("unroll") for (int m = 0; m < 4; ++m) _Pragma("unroll") for (int n = 0; n < 2; ++n) _Pragma("unroll") for (int k = 0; k < 2; ++k) \
;         acc[ai][bj][m][n] = mma16(Bt[n][k], At[m][k], acc[ai][bj][m][n]); __builtin_amdgcn_s_setprio(0); } while (0)
; template <class Epi, class Sched, bool ALIGN_EPI = false, bool SP2 = false>
; __device__ __forceinline__ void gemm_phase(PG8_LAS unsigned char* lds, const Gemm g, const Sched& S, const Epi& E, Stopwatch& sw) {
;     ...
;             const bool last = (t == nt - 2);
;             const char* a1 = cA + (size_t)(t + 1) * kstep;
;             const char* a2 = last ? nA : cA + (size_t)(t + 2) * kstep; const char* b2 = last ? nB : cB + (size_t)(t + 2) * kstep;
;             const char* a3 = a2 + kstep; const char* b3 = b2 + kstep;
;             if (last && has_next) S.a_ready(nxt);
;             if constexpr (SP2) {
;             int relax = __builtin_amdgcn_readfirstlane((int)((ui > 0) && (t == 0))); asm volatile("" : "+s"(relax));
;             PG8_LDB(B0, 0, 0); PG8_LDB(B1, 0, 1); PG8_SCHED; PG8_LDA(At, 0, 0); if (!relax) PG8_STAGE(PG8_SA(1, 1), a1 + hstep, voffA);
;             if (relax) PG8_WAIT_VN(8 + Epi::NST); else PG8_WAIT_V(8); PG8_WAIT_L(0); PG8_BAR; PG8_MMA(0, 0, At, B0); PG8_MMA(0, 1, At, B1); PG8_BAR; PG8_SCHED;
;             PG8_LDA(At, 0, 1); PG8_STAGE(PG8_SB(0, 0), b2, voffB); PG8_STAGE(PG8_SB(0, 1), b2 + hstep, voffB); PG8_STAGE(PG8_SA(0, 0), a2, voffA);
;             if (relax) PG8_WAIT_VN(8 + Epi::NST); else PG8_WAIT_V(8); PG8_WAIT_L(0); PG8_BAR; PG8_MMA(1, 0, At, B0); PG8_MMA(1, 1, At, B1); PG8_BAR; PG8_SCHED;
.LBB0_1231:
	s_add_u32 s40, s56, s60
	s_addc_u32 s41, s57, s61
	s_add_u32 s68, s40, 0x100
	s_addc_u32 s69, s41, 0
	s_add_u32 s62, s76, s60
	s_addc_u32 s63, s77, s61
	s_cmpk_eq_i32 s60, 0x3f00
	s_cselect_b64 s[64:65], -1, 0
	s_waitcnt lgkmcnt(0)
	s_and_b64 s[40:41], s[64:65], exec
	s_cselect_b32 s63, s49, s63
	s_cselect_b32 s62, s91, s62
	s_cselect_b32 s69, s51, s69
	s_cselect_b32 s68, s3, s68
	s_barrier
	s_setprio 1
	s_waitcnt lgkmcnt(0)
	v_mfma_f32_16x16x32_bf16 v[128:131], v[148:151], v[188:191], v[128:131]
	v_mfma_f32_16x16x32_bf16 v[124:127], v[156:159], v[188:191], v[124:127]
	v_mfma_f32_16x16x32_bf16 v[112:115], v[148:151], v[180:183], v[112:115]
	v_mfma_f32_16x16x32_bf16 v[108:111], v[156:159], v[180:183], v[108:111]
	v_mfma_f32_16x16x32_bf16 v[96:99], v[148:151], v[172:175], v[96:99]
	v_mfma_f32_16x16x32_bf16 v[92:95], v[156:159], v[172:175], v[92:95]
	v_mfma_f32_16x16x32_bf16 v[80:83], v[148:151], v[164:167], v[80:83]
	v_mfma_f32_16x16x32_bf16 v[76:79], v[156:159], v[164:167], v[76:79]
	v_mfma_f32_16x16x32_bf16 v[128:131], v[152:155], v[192:195], v[128:131]
	v_mfma_f32_16x16x32_bf16 v[124:127], v[160:163], v[192:195], v[124:127]
	v_mfma_f32_16x16x32_bf16 v[112:115], v[152:155], v[184:187], v[112:115]
	v_mfma_f32_16x16x32_bf16 v[108:111], v[160:163], v[184:187], v[108:111]
	v_mfma_f32_16x16x32_bf16 v[96:99], v[152:155], v[176:179], v[96:99]
	v_mfma_f32_16x16x32_bf16 v[92:95], v[160:163], v[176:179], v[92:95]
	v_mfma_f32_16x16x32_bf16 v[80:83], v[152:155], v[168:171], v[80:83]
	v_mfma_f32_16x16x32_bf16 v[76:79], v[160:163], v[168:171], v[76:79]
	v_mfma_f32_16x16x32_bf16 v[120:123], v[132:135], v[188:191], v[120:123]
	v_mfma_f32_16x16x32_bf16 v[116:119], v[140:143], v[188:191], v[116:119]
	v_mfma_f32_16x16x32_bf16 v[104:107], v[132:135], v[180:183], v[104:107]
	v_mfma_f32_16x16x32_bf16 v[100:103], v[140:143], v[180:183], v[100:103]
	v_mfma_f32_16x16x32_bf16 v[88:91], v[132:135], v[172:175], v[88:91]
	v_mfma_f32_16x16x32_bf16 v[84:87], v[140:143], v[172:175], v[84:87]
	v_mfma_f32_16x16x32_bf16 v[72:75], v[132:135], v[164:167], v[72:75]
	v_mfma_f32_16x16x32_bf16 v[68:71], v[140:143], v[164:167], v[68:71]
	v_mfma_f32_16x16x32_bf16 v[120:123], v[136:139], v[192:195], v[120:123]
	v_mfma_f32_16x16x32_bf16 v[116:119], v[144:147], v[192:195], v[116:119]
	v_mfma_f32_16x16x32_bf16 v[104:107], v[136:139], v[184:187], v[104:107]
	v_mfma_f32_16x16x32_bf16 v[100:103], v[144:147], v[184:187], v[100:103]
	v_mfma_f32_16x16x32_bf16 v[88:91], v[136:139], v[176:179], v[88:91]
	v_mfma_f32_16x16x32_bf16 v[84:87], v[144:147], v[176:179], v[84:87]
	v_mfma_f32_16x16x32_bf16 v[72:75], v[136:139], v[168:171], v[72:75]
	v_mfma_f32_16x16x32_bf16 v[68:71], v[144:147], v[168:171], v[68:71]
	s_setprio 0
	s_barrier
	s_mov_b32 m0, s18
	v_lshl_add_u64 v[218:219], s[62:63], 0, v[2:3]
	s_add_u32 s40, s62, 0x200000
	ds_read_b128 v[188:191], v228 offset:16384
	ds_read_b128 v[192:195], v228 offset:17408
	ds_read_b128 v[180:183], v228 offset:18432
	ds_read_b128 v[184:187], v228 offset:19456
	ds_read_b128 v[172:175], v228 offset:20480
	ds_read_b128 v[176:179], v228 offset:21504
	ds_read_b128 v[164:167], v228 offset:22528
	ds_read_b128 v[168:171], v228 offset:23552
	global_load_lds_dwordx4 v[218:219], off
	v_lshl_add_u64 v[220:221], s[62:63], 0, v[196:197]
	s_mov_b32 m0, s19
	s_addc_u32 s41, s63, 0
	global_load_lds_dwordx4 v[220:221], off
	v_lshl_add_u64 v[222:223], s[40:41], 0, v[2:3]
	s_mov_b32 m0, s24
	v_lshl_add_u64 v[224:225], s[68:69], 0, v[202:203]
	global_load_lds_dwordx4 v[222:223], off
	v_lshl_add_u64 v[222:223], s[40:41], 0, v[196:197]
	s_mov_b32 m0, s25
	v_cndmask_b32_e64 v229, 0, 1, s[74:75]
	global_load_lds_dwordx4 v[222:223], off
	v_lshl_add_u64 v[222:223], s[68:69], 0, v[204:205]
	s_mov_b32 m0, s16
	v_cmp_ne_u32_e64 s[40:41], 1, v229
	global_load_lds_dwordx4 v[222:223], off
	s_mov_b32 m0, s31
	s_andn2_b64 vcc, exec, s[74:75]
	global_load_lds_dwordx4 v[224:225], off
	s_cbranch_vccz .Lrlx_11

; #define PG8_STAGE(bufoff, gbase, voff) do { _Pragma("unroll") for (int _i = 0; _i < 2; ++_i) \
;         __builtin_amdgcn_global_load_lds((const unsigned*)((const char*)(gbase) + (voff)[_i]), (PG8_LAS unsigned*)(lds + (bufoff) + ldsw + _i * 8192), 16, 0, 0); } while (0)
; #define PG8_LDA(dst, b, h) do { _Pragma("unroll") for (int m = 0; m < 4; ++m) _Pragma("unroll") for (int k = 0; k < 2; ++k) dst[m][k] = *(const PG8_LAS bf16x8*)(lds + PG8_SA(b, h) + aoff + m * 2048 + k * 1024); } while (0)
; #define PG8_LDB(dst, b, h) do { _Pragma("unroll") for (int n = 0; n < 2; ++n) _Pragma("unroll") for (int k = 0; k < 2; ++k) dst[n][k] = *(const PG8_LAS bf16x8*)(lds + PG8_SB(b, h) + boff + n * 2048 + k * 1024); } while (0)
; #define PG8_MMA(ai, bj, At, Bt) do { __builtin_amdgcn_s_setprio(1); _Pragma("unroll") for (int m = 0; m < 4; ++m) _Pragma("unroll") for (int n = 0; n < 2; ++n) _Pragma("unroll") for (int k = 0; k < 2; ++k) \
;         acc[ai][bj][m][n] = mma16(Bt[n][k], At[m][k], acc[ai][bj][m][n]); __builtin_amdgcn_s_setprio(0); } while (0)
; #define PG8_WAIT_V(n) asm volatile("s_waitcnt vmcnt(" #n ")" ::: "memory")
; #define PG8_WAIT_VN(n) asm volatile("s_waitcnt vmcnt(%0)" :: "n"(n) : "memory")
; #define PG8_WAIT_L(n) asm volatile("s_waitcnt lgkmcnt(" #n ")" ::: "memory")
; #define PG8_BAR __builtin_amdgcn_s_barrier()
; #define PG8_SCHED __builtin_amdgcn_sched_barrier(0)
; template <class Epi, class Sched, bool ALIGN_EPI = false, bool SP2 = false>
; __device__ __forceinline__ void gemm_phase(PG8_LAS unsigned char* lds, const Gemm g, const Sched& S, const Epi& E, Stopwatch& sw) {
;     ...
;             if (relax) PG8_WAIT_VN(8 + Epi::NST); else PG8_WAIT_V(8); PG8_WAIT_L(0); PG8_BAR; PG8_MMA(1, 0, At, B0); PG8_MMA(1, 1, At, B1); PG8_BAR; PG8_SCHED;
;             PG8_LDB(B0, 1, 0); PG8_LDB(B1, 1, 1); PG8_SCHED; PG8_LDA(At, 1, 0); PG8_STAGE(PG8_SA(0, 1), a2 + hstep, voffA);
;             if (relax) PG8_WAIT_VN(8 + Epi::NST); else PG8_WAIT_V(8); PG8_WAIT_L(0); PG8_BAR; PG8_MMA(0, 0, At, B0); PG8_MMA(0, 1, At, B1); PG8_BAR; PG8_SCHED;
.LBB0_1234:
	s_waitcnt lgkmcnt(0)
	s_barrier
	s_setprio 1
	s_waitcnt lgkmcnt(0)
	v_mfma_f32_16x16x32_bf16 v[64:67], v[148:151], v[188:191], v[64:67]
	v_mfma_f32_16x16x32_bf16 v[60:63], v[156:159], v[188:191], v[60:63]
	v_mfma_f32_16x16x32_bf16 v[48:51], v[148:151], v[180:183], v[48:51]
	v_mfma_f32_16x16x32_bf16 v[44:47], v[156:159], v[180:183], v[44:47]
	v_mfma_f32_16x16x32_bf16 v[32:35], v[148:151], v[172:175], v[32:35]
	v_mfma_f32_16x16x32_bf16 v[28:31], v[156:159], v[172:175], v[28:31]
	v_mfma_f32_16x16x32_bf16 v[16:19], v[148:151], v[164:167], v[16:19]
	v_mfma_f32_16x16x32_bf16 v[12:15], v[156:159], v[164:167], v[12:15]
	v_mfma_f32_16x16x32_bf16 v[64:67], v[152:155], v[192:195], v[64:67]
	v_mfma_f32_16x16x32_bf16 v[60:63], v[160:163], v[192:195], v[60:63]
	v_mfma_f32_16x16x32_bf16 v[48:51], v[152:155], v[184:187], v[48:51]
	v_mfma_f32_16x16x32_bf16 v[44:47], v[160:163], v[184:187], v[44:47]
	v_mfma_f32_16x16x32_bf16 v[32:35], v[152:155], v[176:179], v[32:35]
	v_mfma_f32_16x16x32_bf16 v[28:31], v[160:163], v[176:179], v[28:31]
	v_mfma_f32_16x16x32_bf16 v[16:19], v[152:155], v[168:171], v[16:19]
	v_mfma_f32_16x16x32_bf16 v[12:15], v[160:163], v[168:171], v[12:15]
	v_mfma_f32_16x16x32_bf16 v[56:59], v[132:135], v[188:191], v[56:59]
	v_mfma_f32_16x16x32_bf16 v[52:55], v[140:143], v[188:191], v[52:55]
	v_mfma_f32_16x16x32_bf16 v[40:43], v[132:135], v[180:183], v[40:43]
	v_mfma_f32_16x16x32_bf16 v[36:39], v[140:143], v[180:183], v[36:39]
	v_mfma_f32_16x16x32_bf16 v[24:27], v[132:135], v[172:175], v[24:27]
	v_mfma_f32_16x16x32_bf16 v[20:23], v[140:143], v[172:175], v[20:23]
	v_mfma_f32_16x16x32_bf16 v[8:11], v[132:135], v[164:167], v[8:11]
	v_mfma_f32_16x16x32_bf16 v[4:7], v[140:143], v[164:167], v[4:7]
	v_mfma_f32_16x16x32_bf16 v[56:59], v[136:139], v[192:195], v[56:59]
	v_mfma_f32_16x16x32_bf16 v[52:55], v[144:147], v[192:195], v[52:55]
	v_mfma_f32_16x16x32_bf16 v[40:43], v[136:139], v[184:187], v[40:43]
	v_mfma_f32_16x16x32_bf16 v[36:39], v[144:147], v[184:187], v[36:39]
	v_mfma_f32_16x16x32_bf16 v[24:27], v[136:139], v[176:179], v[24:27]
	v_mfma_f32_16x16x32_bf16 v[20:23], v[144:147], v[176:179], v[20:23]
	v_mfma_f32_16x16x32_bf16 v[8:11], v[136:139], v[168:171], v[8:11]
	v_mfma_f32_16x16x32_bf16 v[4:7], v[144:147], v[168:171], v[4:7]
	s_setprio 0
	s_barrier
	v_add_u32_e32 v132, 0x18000, v227
	v_add_u32_e32 v144, 0x1c000, v227
	ds_read_b128 v[148:151], v132
	ds_read_b128 v[152:155], v132 offset:1024
	ds_read_b128 v[156:159], v132 offset:2048
	ds_read_b128 v[160:163], v132 offset:3072
	ds_read_b128 v[132:135], v144
	ds_read_b128 v[136:139], v144 offset:1024
	ds_read_b128 v[140:143], v144 offset:2048
	ds_read_b128 v[144:147], v144 offset:3072
	s_add_u32 s68, s68, 0x200000
	s_addc_u32 s69, s69, 0
	s_mov_b32 m0, s72
	v_lshl_add_u64 v[230:231], s[68:69], 0, v[204:205]
	ds_read_b128 v[188:191], v228 offset:32768
	ds_read_b128 v[192:195], v228 offset:33792
	ds_read_b128 v[180:183], v228 offset:34816
	ds_read_b128 v[184:187], v228 offset:35840
	ds_read_b128 v[172:175], v228 offset:36864
	ds_read_b128 v[176:179], v228 offset:37888
	ds_read_b128 v[164:167], v228 offset:38912
	ds_read_b128 v[168:171], v228 offset:39936
	global_load_lds_dwordx4 v[230:231], off
	v_lshl_add_u64 v[230:231], s[68:69], 0, v[202:203]
	s_mov_b32 m0, s73
	s_and_b64 vcc, exec, s[40:41]
	global_load_lds_dwordx4 v[230:231], off
	s_mov_b64 s[74:75], s[10:11]
	s_cbranch_vccz .Lrlx_12
